# v37
# speedup vs baseline: 1.0052x; 1.0052x over previous
.LBB0_9:
	s_add_i32 s26, s35, 8
	s_cmpk_lt_i32 s26, 0x80
	s_cbranch_scc0 .Lp1_last_top
	s_lshl_b32 s24, s26, 14
	s_add_i32 s24, s24, s33
	s_waitcnt vmcnt(15)
	v_cvt_pk_bf16_f32 v2, v34, v35
	v_cvt_pk_bf16_f32 v3, v36, v37
	s_waitcnt vmcnt(11)
	v_cvt_pk_bf16_f32 v10, v50, v51
	v_cvt_pk_bf16_f32 v11, v52, v53
	v_cvt_pk_bf16_f32 v4, v38, v39
	v_cvt_pk_bf16_f32 v5, v40, v41
	ds_write2_b64 v212, v[2:3], v[10:11] offset1:68
	s_waitcnt vmcnt(10)
	v_cvt_pk_bf16_f32 v2, v54, v55
	v_cvt_pk_bf16_f32 v3, v56, v57
	v_cvt_pk_bf16_f32 v6, v42, v43
	v_cvt_pk_bf16_f32 v7, v44, v45
	ds_write2_b64 v215, v[4:5], v[2:3] offset0:16 offset1:84
	s_waitcnt vmcnt(9)
	v_cvt_pk_bf16_f32 v2, v58, v59
	v_cvt_pk_bf16_f32 v3, v60, v61
	v_cvt_pk_bf16_f32 v8, v46, v47
	v_cvt_pk_bf16_f32 v9, v48, v49
	ds_write2_b64 v216, v[6:7], v[2:3] offset0:32 offset1:100
	s_waitcnt vmcnt(8)
	v_cvt_pk_bf16_f32 v2, v62, v63
	v_cvt_pk_bf16_f32 v3, v64, v65
	ds_write2_b64 v217, v[8:9], v[2:3] offset0:48 offset1:116
	s_or_b32 s25, s24, 0x1000
	buffer_load_dwordx4 v[34:37], v204, s[12:15], s24 offen sc0 nt sc1
	buffer_load_dwordx4 v[38:41], v204, s[12:15], s25 offen sc0 nt sc1
	s_or_b32 s25, s24, 0x2000
	s_or_b32 s27, s24, 0x3000
	buffer_load_dwordx4 v[42:45], v204, s[12:15], s25 offen sc0 nt sc1
	buffer_load_dwordx4 v[46:49], v204, s[12:15], s27 offen sc0 nt sc1
	s_or_b32 s25, s24, 0x400
	s_or_b32 s27, s24, 0x1400
	buffer_load_dwordx4 v[50:53], v204, s[12:15], s25 offen sc0 nt sc1
	buffer_load_dwordx4 v[54:57], v204, s[12:15], s27 offen sc0 nt sc1
	s_or_b32 s25, s24, 0x2400
	s_or_b32 s27, s24, 0x3400
	buffer_load_dwordx4 v[58:61], v204, s[12:15], s25 offen sc0 nt sc1
	buffer_load_dwordx4 v[62:65], v204, s[12:15], s27 offen sc0 nt sc1
	s_waitcnt vmcnt(15)
	v_cvt_pk_bf16_f32 v2, v66, v67
	v_cvt_pk_bf16_f32 v3, v68, v69
	s_waitcnt vmcnt(11)
	v_cvt_pk_bf16_f32 v10, v82, v83
	v_cvt_pk_bf16_f32 v11, v84, v85
	v_cvt_pk_bf16_f32 v4, v70, v71
	v_cvt_pk_bf16_f32 v5, v72, v73
	ds_write2_b64 v212, v[2:3], v[10:11] offset0:136 offset1:204
	s_waitcnt vmcnt(10)
	v_cvt_pk_bf16_f32 v2, v86, v87
	v_cvt_pk_bf16_f32 v3, v88, v89
	v_cvt_pk_bf16_f32 v6, v74, v75
	v_cvt_pk_bf16_f32 v7, v76, v77
	ds_write2_b64 v215, v[4:5], v[2:3] offset0:152 offset1:220
	s_waitcnt vmcnt(9)
	v_cvt_pk_bf16_f32 v2, v90, v91
	v_cvt_pk_bf16_f32 v3, v92, v93
	v_cvt_pk_bf16_f32 v8, v78, v79
	v_cvt_pk_bf16_f32 v9, v80, v81
	ds_write2_b64 v216, v[6:7], v[2:3] offset0:168 offset1:236
	s_waitcnt vmcnt(8)
	v_cvt_pk_bf16_f32 v2, v94, v95
	v_cvt_pk_bf16_f32 v3, v96, v97
	ds_write2_b64 v217, v[8:9], v[2:3] offset0:184 offset1:252
	s_or_b32 s25, s24, 0x800
	s_or_b32 s27, s24, 0x1800
	buffer_load_dwordx4 v[66:69], v204, s[12:15], s25 offen sc0 nt sc1
	buffer_load_dwordx4 v[70:73], v204, s[12:15], s27 offen sc0 nt sc1
	s_or_b32 s25, s24, 0x2800
	s_or_b32 s27, s24, 0x3800
	buffer_load_dwordx4 v[74:77], v204, s[12:15], s25 offen sc0 nt sc1
	buffer_load_dwordx4 v[78:81], v204, s[12:15], s27 offen sc0 nt sc1
	s_or_b32 s25, s24, 0xc00
	s_or_b32 s27, s24, 0x1c00
	buffer_load_dwordx4 v[82:85], v204, s[12:15], s25 offen sc0 nt sc1
	buffer_load_dwordx4 v[86:89], v204, s[12:15], s27 offen sc0 nt sc1
	s_or_b32 s25, s24, 0x2c00
	s_or_b32 s24, s24, 0x3c00
	buffer_load_dwordx4 v[90:93], v204, s[12:15], s25 offen sc0 nt sc1
	buffer_load_dwordx4 v[94:97], v204, s[12:15], s24 offen sc0 nt sc1
	s_branch .LBB0_17
